# speedup vs baseline: 1.0042x; 1.0042x over previous
_Z8reduce_kPKDF16_PKfPf:
	s_load_dwordx4 s[4:7], s[0:1], 0x0
	s_load_dwordx2 s[8:9], s[0:1], 0x10
	v_lshlrev_b32_e32 v1, 3, v0
	v_and_b32_e32 v18, 7, v0
	v_lshrrev_b32_e32 v19, 4, v0
	v_lshlrev_b32_e32 v18, 4, v18
	v_lshl_or_b32 v18, v19, 7, v18
	v_bfe_u32 v19, v0, 3, 1
	v_lshl_or_b32 v19, v19, 12, v18
	s_lshl_b32 s3, s2, 12
	s_lshl_b32 s2, s2, 13
	s_waitcnt lgkmcnt(0)
	s_add_u32 s4, s4, s3
	s_addc_u32 s5, s5, 0
	s_add_u32 s10, s4, 0x800000
	s_addc_u32 s11, s5, 0
	s_add_u32 s12, s4, 0x1000000
	s_addc_u32 s13, s5, 0
	s_add_u32 s14, s4, 0x1800000
	s_addc_u32 s15, s5, 0
	s_add_u32 s8, s8, s2
	s_addc_u32 s9, s9, 0
	global_load_dwordx2 v[2:3], v1, s[4:5] nt
	global_load_dwordx2 v[4:5], v1, s[10:11] nt
	global_load_dwordx2 v[6:7], v1, s[12:13] nt
	global_load_dwordx2 v[8:9], v1, s[14:15] nt
	global_load_dwordx4 v[20:23], v18, s[6:7]
	global_load_dwordx2 v[10:11], v1, s[4:5] offset:2048 nt
	global_load_dwordx2 v[12:13], v1, s[10:11] offset:2048 nt
	global_load_dwordx2 v[14:15], v1, s[12:13] offset:2048 nt
	global_load_dwordx2 v[16:17], v1, s[14:15] offset:2048 nt
	global_load_dwordx4 v[24:27], v18, s[6:7] offset:2048
	s_mov_b32 s0, 0x41800000
	s_waitcnt vmcnt(5)
	v_cvt_f32_f16_e32 v28, v2
	v_cvt_f32_f16_sdwa v29, v2 dst_sel:DWORD dst_unused:UNUSED_PAD src0_sel:WORD_1
	v_cvt_f32_f16_e32 v30, v3
	v_cvt_f32_f16_sdwa v31, v3 dst_sel:DWORD dst_unused:UNUSED_PAD src0_sel:WORD_1
	v_cvt_f32_f16_e32 v32, v4
	v_cvt_f32_f16_sdwa v33, v4 dst_sel:DWORD dst_unused:UNUSED_PAD src0_sel:WORD_1
	v_cvt_f32_f16_e32 v34, v5
	v_cvt_f32_f16_sdwa v35, v5 dst_sel:DWORD dst_unused:UNUSED_PAD src0_sel:WORD_1
	v_pk_add_f32 v[28:29], v[28:29], v[32:33]
	v_pk_add_f32 v[30:31], v[30:31], v[34:35]
	v_cvt_f32_f16_e32 v32, v6
	v_cvt_f32_f16_sdwa v33, v6 dst_sel:DWORD dst_unused:UNUSED_PAD src0_sel:WORD_1
	v_cvt_f32_f16_e32 v34, v7
	v_cvt_f32_f16_sdwa v35, v7 dst_sel:DWORD dst_unused:UNUSED_PAD src0_sel:WORD_1
	v_pk_add_f32 v[28:29], v[28:29], v[32:33]
	v_pk_add_f32 v[30:31], v[30:31], v[34:35]
	v_cvt_f32_f16_e32 v32, v8
	v_cvt_f32_f16_sdwa v33, v8 dst_sel:DWORD dst_unused:UNUSED_PAD src0_sel:WORD_1
	v_cvt_f32_f16_e32 v34, v9
	v_cvt_f32_f16_sdwa v35, v9 dst_sel:DWORD dst_unused:UNUSED_PAD src0_sel:WORD_1
	v_pk_add_f32 v[28:29], v[28:29], v[32:33]
	v_pk_add_f32 v[30:31], v[30:31], v[34:35]
	v_pk_fma_f32 v[20:21], v[28:29], s[0:1], v[20:21] op_sel_hi:[1,0,1]
	v_pk_fma_f32 v[22:23], v[30:31], s[0:1], v[22:23] op_sel_hi:[1,0,1]
	s_waitcnt vmcnt(0)
	v_cvt_f32_f16_e32 v28, v10
	v_cvt_f32_f16_sdwa v29, v10 dst_sel:DWORD dst_unused:UNUSED_PAD src0_sel:WORD_1
	v_cvt_f32_f16_e32 v30, v11
	v_cvt_f32_f16_sdwa v31, v11 dst_sel:DWORD dst_unused:UNUSED_PAD src0_sel:WORD_1
	v_cvt_f32_f16_e32 v32, v12
	v_cvt_f32_f16_sdwa v33, v12 dst_sel:DWORD dst_unused:UNUSED_PAD src0_sel:WORD_1
	v_cvt_f32_f16_e32 v34, v13
	v_cvt_f32_f16_sdwa v35, v13 dst_sel:DWORD dst_unused:UNUSED_PAD src0_sel:WORD_1
	v_pk_add_f32 v[28:29], v[28:29], v[32:33]
	v_pk_add_f32 v[30:31], v[30:31], v[34:35]
	v_cvt_f32_f16_e32 v32, v14
	v_cvt_f32_f16_sdwa v33, v14 dst_sel:DWORD dst_unused:UNUSED_PAD src0_sel:WORD_1
	v_cvt_f32_f16_e32 v34, v15
	v_cvt_f32_f16_sdwa v35, v15 dst_sel:DWORD dst_unused:UNUSED_PAD src0_sel:WORD_1
	v_pk_add_f32 v[28:29], v[28:29], v[32:33]
	v_pk_add_f32 v[30:31], v[30:31], v[34:35]
	v_cvt_f32_f16_e32 v32, v16
	v_cvt_f32_f16_sdwa v33, v16 dst_sel:DWORD dst_unused:UNUSED_PAD src0_sel:WORD_1
	v_cvt_f32_f16_e32 v34, v17
	v_cvt_f32_f16_sdwa v35, v17 dst_sel:DWORD dst_unused:UNUSED_PAD src0_sel:WORD_1
	v_pk_add_f32 v[28:29], v[28:29], v[32:33]
	v_pk_add_f32 v[30:31], v[30:31], v[34:35]
	v_pk_fma_f32 v[24:25], v[28:29], s[0:1], v[24:25] op_sel_hi:[1,0,1]
	v_pk_fma_f32 v[26:27], v[30:31], s[0:1], v[26:27] op_sel_hi:[1,0,1]
	global_store_dwordx4 v19, v[20:23], s[8:9] nt
	global_store_dwordx4 v19, v[24:27], s[8:9] offset:2048 nt
	s_endpgm

	.amdhsa_kernel _Z8reduce_kPKDF16_PKfPf
		.amdhsa_group_segment_fixed_size 0
		.amdhsa_private_segment_fixed_size 0
		.amdhsa_kernarg_size 280
		.amdhsa_user_sgpr_count 2
		.amdhsa_user_sgpr_dispatch_ptr 0
		.amdhsa_user_sgpr_queue_ptr 0
		.amdhsa_user_sgpr_kernarg_segment_ptr 1
		.amdhsa_user_sgpr_dispatch_id 0
		.amdhsa_user_sgpr_kernarg_preload_length 0
		.amdhsa_user_sgpr_kernarg_preload_offset 0
		.amdhsa_user_sgpr_private_segment_size 0
		.amdhsa_uses_dynamic_stack 0
		.amdhsa_enable_private_segment 0
		.amdhsa_system_sgpr_workgroup_id_x 1
		.amdhsa_system_sgpr_workgroup_id_y 0
		.amdhsa_system_sgpr_workgroup_id_z 0
		.amdhsa_system_sgpr_workgroup_info 0
		.amdhsa_system_vgpr_workitem_id 0
		.amdhsa_next_free_vgpr 42
		.amdhsa_next_free_sgpr 16
		.amdhsa_accum_offset 44
		.amdhsa_reserve_vcc 1
		.amdhsa_float_round_mode_32 0
		.amdhsa_float_round_mode_16_64 0
		.amdhsa_float_denorm_mode_32 3
		.amdhsa_float_denorm_mode_16_64 3
		.amdhsa_dx10_clamp 1
		.amdhsa_ieee_mode 1
		.amdhsa_fp16_overflow 0
		.amdhsa_tg_split 0
		.amdhsa_exception_fp_ieee_invalid_op 0
		.amdhsa_exception_fp_denorm_src 0
		.amdhsa_exception_fp_ieee_div_zero 0
		.amdhsa_exception_fp_ieee_overflow 0
		.amdhsa_exception_fp_ieee_underflow 0
		.amdhsa_exception_fp_ieee_inexact 0
		.amdhsa_exception_int_div_zero 0
	.end_amdhsa_kernel

amdhsa.kernels:
  - .agpr_count:     0
    .args:
      - .actual_access:  read_only
        .address_space:  global
        .offset:         0
        .size:           8
        .value_kind:     global_buffer
      - .actual_access:  read_only
        .address_space:  global
        .offset:         8
        .size:           8
        .value_kind:     global_buffer
      - .actual_access:  read_only
        .address_space:  global
        .offset:         16
        .size:           8
        .value_kind:     global_buffer
      - .actual_access:  write_only
        .address_space:  global
        .offset:         24
        .size:           8
        .value_kind:     global_buffer
      - .actual_access:  write_only
        .address_space:  global
        .offset:         32
        .size:           8
        .value_kind:     global_buffer
      - .actual_access:  write_only
        .address_space:  global
        .offset:         40
        .size:           8
        .value_kind:     global_buffer
      - .actual_access:  write_only
        .address_space:  global
        .offset:         48
        .size:           8
        .value_kind:     global_buffer
      - .actual_access:  read_only
        .address_space:  global
        .offset:         56
        .size:           8
        .value_kind:     global_buffer
      - .actual_access:  read_only
        .address_space:  global
        .offset:         64
        .size:           8
        .value_kind:     global_buffer
      - .actual_access:  write_only
        .address_space:  global
        .offset:         72
        .size:           8
        .value_kind:     global_buffer
    .group_segment_fixed_size: 8448
    .kernarg_segment_align: 8
    .kernarg_segment_size: 80
    .language:       OpenCL C
    .language_version:
      - 2
      - 0
    .max_flat_workgroup_size: 256
    .name:           _Z6prep_kPKfS0_S0_PDF16_S1_S1_S1_S1_S0_Pf
    .private_segment_fixed_size: 0
    .sgpr_count:     22
    .sgpr_spill_count: 0
    .symbol:         _Z6prep_kPKfS0_S0_PDF16_S1_S1_S1_S1_S0_Pf.kd
    .uniform_work_group_size: 1
    .uses_dynamic_stack: false
    .vgpr_count:     34
    .vgpr_spill_count: 0
    .wavefront_size: 64
  - .agpr_count:     0
    .args:
      - .actual_access:  read_only
        .address_space:  global
        .offset:         0
        .size:           8
        .value_kind:     global_buffer
      - .actual_access:  write_only
        .address_space:  global
        .offset:         8
        .size:           8
        .value_kind:     global_buffer
      - .actual_access:  read_only
        .address_space:  global
        .offset:         16
        .size:           8
        .value_kind:     global_buffer
      - .actual_access:  write_only
        .address_space:  global
        .offset:         24
        .size:           8
        .value_kind:     global_buffer
      - .offset:         32
        .size:           4
        .value_kind:     hidden_block_count_x
      - .offset:         36
        .size:           4
        .value_kind:     hidden_block_count_y
      - .offset:         40
        .size:           4
        .value_kind:     hidden_block_count_z
      - .offset:         44
        .size:           2
        .value_kind:     hidden_group_size_x
      - .offset:         46
        .size:           2
        .value_kind:     hidden_group_size_y
      - .offset:         48
        .size:           2
        .value_kind:     hidden_group_size_z
      - .offset:         50
        .size:           2
        .value_kind:     hidden_remainder_x
      - .offset:         52
        .size:           2
        .value_kind:     hidden_remainder_y
      - .offset:         54
        .size:           2
        .value_kind:     hidden_remainder_z
      - .offset:         72
        .size:           8
        .value_kind:     hidden_global_offset_x
      - .offset:         80
        .size:           8
        .value_kind:     hidden_global_offset_y
      - .offset:         88
        .size:           8
        .value_kind:     hidden_global_offset_z
      - .offset:         96
        .size:           2
        .value_kind:     hidden_grid_dims
    .group_segment_fixed_size: 0
    .kernarg_segment_align: 8
    .kernarg_segment_size: 288
    .language:       OpenCL C
    .language_version:
      - 2
      - 0
    .max_flat_workgroup_size: 1024
    .name:           _Z6post_kPKfPfPKDF16_PDF16_
    .private_segment_fixed_size: 0
    .sgpr_count:     14
    .sgpr_spill_count: 0
    .symbol:         _Z6post_kPKfPfPKDF16_PDF16_.kd
    .uniform_work_group_size: 1
    .uses_dynamic_stack: false
    .vgpr_count:     49
    .vgpr_spill_count: 0
    .wavefront_size: 64
  - .agpr_count:     0
    .args:
      - .actual_access:  read_only
        .address_space:  global
        .offset:         0
        .size:           8
        .value_kind:     global_buffer
      - .actual_access:  read_only
        .address_space:  global
        .offset:         8
        .size:           8
        .value_kind:     global_buffer
      - .actual_access:  write_only
        .address_space:  global
        .offset:         16
        .size:           8
        .value_kind:     global_buffer
      - .offset:         24
        .size:           4
        .value_kind:     hidden_block_count_x
      - .offset:         28
        .size:           4
        .value_kind:     hidden_block_count_y
      - .offset:         32
        .size:           4
        .value_kind:     hidden_block_count_z
      - .offset:         36
        .size:           2
        .value_kind:     hidden_group_size_x
      - .offset:         38
        .size:           2
        .value_kind:     hidden_group_size_y
      - .offset:         40
        .size:           2
        .value_kind:     hidden_group_size_z
      - .offset:         42
        .size:           2
        .value_kind:     hidden_remainder_x
      - .offset:         44
        .size:           2
        .value_kind:     hidden_remainder_y
      - .offset:         46
        .size:           2
        .value_kind:     hidden_remainder_z
      - .offset:         64
        .size:           8
        .value_kind:     hidden_global_offset_x
      - .offset:         72
        .size:           8
        .value_kind:     hidden_global_offset_y
      - .offset:         80
        .size:           8
        .value_kind:     hidden_global_offset_z
      - .offset:         88
        .size:           2
        .value_kind:     hidden_grid_dims
    .group_segment_fixed_size: 0
    .kernarg_segment_align: 8
    .kernarg_segment_size: 280
    .language:       OpenCL C
    .language_version:
      - 2
      - 0
    .max_flat_workgroup_size: 1024
    .name:           _Z8reduce_kPKDF16_PKfPf
    .private_segment_fixed_size: 0
    .sgpr_count:     22
    .sgpr_spill_count: 0
    .symbol:         _Z8reduce_kPKDF16_PKfPf.kd
    .uniform_work_group_size: 1
    .uses_dynamic_stack: false
    .vgpr_count:     42
    .vgpr_spill_count: 0
    .wavefront_size: 64
  - .agpr_count:     0
    .args:
      - .actual_access:  read_only
        .address_space:  global
        .offset:         0
        .size:           8
        .value_kind:     global_buffer
      - .actual_access:  read_only
        .address_space:  global
        .offset:         8
        .size:           8
        .value_kind:     global_buffer
      - .actual_access:  write_only
        .address_space:  global
        .offset:         16
        .size:           8
        .value_kind:     global_buffer
      - .address_space:  global
        .offset:         24
        .size:           8
        .value_kind:     global_buffer
      - .actual_access:  write_only
        .address_space:  global
        .offset:         32
        .size:           8
        .value_kind:     global_buffer
      - .actual_access:  read_only
        .address_space:  global
        .offset:         40
        .size:           8
        .value_kind:     global_buffer
      - .actual_access:  write_only
        .address_space:  global
        .offset:         48
        .size:           8
        .value_kind:     global_buffer
    .group_segment_fixed_size: 0
    .kernarg_segment_align: 8
    .kernarg_segment_size: 56
    .language:       OpenCL C
    .language_version:
      - 2
      - 0
    .max_flat_workgroup_size: 512
    .name:           _Z7gemm1_kPKDF16_S0_PDF16_PKfPfS0_S1_
    .private_segment_fixed_size: 0
    .sgpr_count:     74
    .sgpr_spill_count: 0
    .symbol:         _Z7gemm1_kPKDF16_S0_PDF16_PKfPfS0_S1_.kd
    .uniform_work_group_size: 1
    .uses_dynamic_stack: false
    .vgpr_count:     244
    .vgpr_spill_count: 0
    .wavefront_size: 64
  - .agpr_count:     0
    .args:
      - .actual_access:  read_only
        .address_space:  global
        .offset:         0
        .size:           8
        .value_kind:     global_buffer
      - .actual_access:  read_only
        .address_space:  global
        .offset:         8
        .size:           8
        .value_kind:     global_buffer
      - .offset:         16
        .size:           4
        .value_kind:     by_value
      - .offset:         20
        .size:           4
        .value_kind:     by_value
      - .offset:         24
        .size:           4
        .value_kind:     by_value
      - .offset:         28
        .size:           4
        .value_kind:     by_value
      - .actual_access:  read_only
        .address_space:  global
        .offset:         32
        .size:           8
        .value_kind:     global_buffer
      - .actual_access:  write_only
        .address_space:  global
        .offset:         40
        .size:           8
        .value_kind:     global_buffer
      - .actual_access:  read_only
        .address_space:  global
        .offset:         48
        .size:           8
        .value_kind:     global_buffer
      - .actual_access:  read_only
        .address_space:  global
        .offset:         56
        .size:           8
        .value_kind:     global_buffer
    .group_segment_fixed_size: 0
    .kernarg_segment_align: 8
    .kernarg_segment_size: 64
    .language:       OpenCL C
    .language_version:
      - 2
      - 0
    .max_flat_workgroup_size: 512
    .name:           _Z6gemm_kILi2EEvPKDF16_S1_iiiiPfPDF16_PKfS2_
    .private_segment_fixed_size: 0
    .sgpr_count:     70
    .sgpr_spill_count: 0
    .symbol:         _Z6gemm_kILi2EEvPKDF16_S1_iiiiPfPDF16_PKfS2_.kd
    .uniform_work_group_size: 1
    .uses_dynamic_stack: false
    .vgpr_count:     224
    .vgpr_spill_count: 0
    .wavefront_size: 64
  - .agpr_count:     0
    .args:
      - .actual_access:  read_only
        .address_space:  global
        .offset:         0
        .size:           8
        .value_kind:     global_buffer
      - .actual_access:  read_only
        .address_space:  global
        .offset:         8
        .size:           8
        .value_kind:     global_buffer
      - .offset:         16
        .size:           4
        .value_kind:     by_value
      - .offset:         20
        .size:           4
        .value_kind:     by_value
      - .offset:         24
        .size:           4
        .value_kind:     by_value
      - .offset:         28
        .size:           4
        .value_kind:     by_value
      - .actual_access:  read_only
        .address_space:  global
        .offset:         32
        .size:           8
        .value_kind:     global_buffer
      - .actual_access:  write_only
        .address_space:  global
        .offset:         40
        .size:           8
        .value_kind:     global_buffer
      - .actual_access:  read_only
        .address_space:  global
        .offset:         48
        .size:           8
        .value_kind:     global_buffer
      - .actual_access:  read_only
        .address_space:  global
        .offset:         56
        .size:           8
        .value_kind:     global_buffer
    .group_segment_fixed_size: 0
    .kernarg_segment_align: 8
    .kernarg_segment_size: 64
    .language:       OpenCL C
    .language_version:
      - 2
      - 0
    .max_flat_workgroup_size: 512
    .name:           _Z6gemm_kILi3EEvPKDF16_S1_iiiiPfPDF16_PKfS2_
    .private_segment_fixed_size: 0
    .sgpr_count:     51
    .sgpr_spill_count: 0
    .symbol:         _Z6gemm_kILi3EEvPKDF16_S1_iiiiPfPDF16_PKfS2_.kd
    .uniform_work_group_size: 1
    .uses_dynamic_stack: false
    .vgpr_count:     220
    .vgpr_spill_count: 0
    .wavefront_size: 64
